# baseline (speedup 1.0000x reference)
.LBB1_1:
	v_mfma_f32_32x32x64_f8f6f4 v[76:91], v[84:91], v[116:123], v[36:51]
	v_cvt_pk_fp8_f32 v132, v161, v163
	v_add_u32_e32 v68, s36, v176
	v_cvt_pk_fp8_f32 v132, v162, v164 op_sel:[0,0,1]
	ds_read_b128 v[162:165], v68 offset:49152
	ds_read_b128 v[166:169], v68 offset:50176
	v_cvt_pk_fp8_f32 v133, v150, v154
	v_cvt_pk_fp8_f32 v133, v152, v157 op_sel:[0,0,1]
	s_lshl_b32 s16, s12, 12
	s_add_i32 s15, s16, 0x3000
	s_add_i32 s17, s14, s33
	s_mov_b32 m0, s17
	s_nop 0
	buffer_load_dwordx4 v174, s[20:23], s15 offen lds
	v_cvt_pk_fp8_f32 v134, v149, v153
	v_cvt_pk_fp8_f32 v134, v151, v156 op_sel:[0,0,1]
	v_cvt_pk_fp8_f32 v135, v155, v159
	v_cvt_pk_fp8_f32 v135, v158, v160 op_sel:[0,0,1]
	v_cvt_pk_fp8_f32 v136, v100, v148
	v_cvt_pk_fp8_f32 v136, v101, v102 op_sel:[0,0,1]
	s_waitcnt lgkmcnt(2)
	v_mfma_f32_32x32x64_f8f6f4 v[92:107], v[92:99], v[116:123], v[36:51]
	ds_read_b128 v[148:151], v68 offset:49664
	ds_read_b128 v[152:155], v68 offset:50688
	v_cvt_pk_fp8_f32 v137, v143, v146
	v_cvt_pk_fp8_f32 v137, v145, v147 op_sel:[0,0,1]
	s_add_i32 s15, s16, 0x1000
	s_add_i32 s17, s13, s34
	s_mov_b32 m0, s17
	s_nop 0
	buffer_load_dwordx4 v174, s[24:27], s15 offen lds
	v_cvt_pk_fp8_f32 v138, v69, v109
	v_cvt_pk_fp8_f32 v138, v108, v142 op_sel:[0,0,1]
	v_cvt_pk_fp8_f32 v139, v110, v144
	v_cvt_pk_fp8_f32 v139, v111, v114 op_sel:[0,0,1]
	s_waitcnt lgkmcnt(2)
	s_nop 0
	v_mfma_f32_32x32x64_f8f6f4 v[4:19], v[162:169], v[132:139], v[4:19]
	v_exp_f32_e32 v142, v76
	v_exp_f32_e32 v143, v77
	v_exp_f32_e32 v144, v78
	v_exp_f32_e32 v145, v79
	v_exp_f32_e32 v146, v80
	v_exp_f32_e32 v147, v81
	v_exp_f32_e32 v156, v82
	v_exp_f32_e32 v157, v83
	v_add_u32_e32 v158, s13, v176
	ds_read_b128 v[108:111], v158
	ds_read_b128 v[112:115], v158 offset:1024
	ds_read_b128 v[52:55], v158 offset:512
	ds_read_b128 v[56:59], v158 offset:1536
	v_exp_f32_e32 v159, v84
	v_exp_f32_e32 v160, v85
	v_mfma_f32_16x16x128_f8f6f4 v[200:203], v[124:131], v[132:139], v[200:203]
	v_exp_f32_e32 v161, v86
	v_exp_f32_e32 v162, v87
	v_exp_f32_e32 v163, v88
	v_exp_f32_e32 v164, v89
	v_exp_f32_e32 v165, v90
	v_exp_f32_e32 v166, v91
	s_waitcnt lgkmcnt(4)
	v_mfma_f32_32x32x64_f8f6f4 v[20:35], v[148:155], v[132:139], v[20:35]
	v_exp_f32_e32 v167, v92
	v_exp_f32_e32 v168, v93
	v_exp_f32_e32 v169, v94
	v_exp_f32_e32 v170, v95
	v_exp_f32_e32 v148, v96
	v_exp_f32_e32 v149, v97
	v_exp_f32_e32 v150, v98
	v_exp_f32_e32 v151, v99
	v_exp_f32_e32 v152, v100
	v_exp_f32_e32 v153, v101
	v_exp_f32_e32 v154, v102
	v_exp_f32_e32 v155, v103
	v_exp_f32_e32 v158, v104
	v_exp_f32_e32 v171, v105
	v_exp_f32_e32 v177, v106
	v_exp_f32_e32 v186, v107
	s_add_i32 s15, s13, 0x4000
	s_cmpk_lg_u32 s13, 0x8000
	s_cselect_b32 s15, s15, 0
	s_waitcnt vmcnt(2) lgkmcnt(0)
	s_barrier
	v_mfma_f32_32x32x64_f8f6f4 v[84:99], v[108:115], v[116:123], v[36:51]
	v_cvt_pk_fp8_f32 v132, v142, v143
	v_add_u32_e32 v142, s14, v176
	v_cvt_pk_fp8_f32 v132, v144, v145 op_sel:[0,0,1]
	ds_read_b128 v[60:63], v142 offset:49152
	ds_read_b128 v[64:67], v142 offset:50176
	v_cvt_pk_fp8_f32 v133, v146, v147
	v_cvt_pk_fp8_f32 v133, v156, v157 op_sel:[0,0,1]
	s_add_i32 s14, s16, 0x4000
	s_add_i32 s17, s13, s33
	s_mov_b32 m0, s17
	s_nop 0
	buffer_load_dwordx4 v174, s[20:23], s14 offen lds
	v_cvt_pk_fp8_f32 v134, v159, v160
	v_cvt_pk_fp8_f32 v134, v161, v162 op_sel:[0,0,1]
	v_cvt_pk_fp8_f32 v135, v163, v164
	v_cvt_pk_fp8_f32 v135, v165, v166 op_sel:[0,0,1]
	s_waitcnt lgkmcnt(2)
	v_mfma_f32_32x32x64_f8f6f4 v[100:115], v[52:59], v[116:123], v[36:51]
	v_cvt_pk_fp8_f32 v136, v167, v168
	v_cvt_pk_fp8_f32 v136, v169, v170 op_sel:[0,0,1]
	ds_read_b128 v[178:181], v142 offset:49664
	ds_read_b128 v[182:185], v142 offset:50688
	v_cvt_pk_fp8_f32 v137, v148, v149
	v_cvt_pk_fp8_f32 v137, v150, v151 op_sel:[0,0,1]
	s_addk_i32 s16, 0x2000
	s_add_i32 s14, s15, s34
	s_mov_b32 m0, s14
	s_nop 0
	buffer_load_dwordx4 v174, s[24:27], s16 offen lds
	v_cvt_pk_fp8_f32 v138, v152, v153
	v_cvt_pk_fp8_f32 v138, v154, v155 op_sel:[0,0,1]
	v_cvt_pk_fp8_f32 v139, v158, v171
	v_cvt_pk_fp8_f32 v139, v177, v186 op_sel:[0,0,1]
	v_sub_f32_e32 v52, v200, v204
	v_mov_b32_e32 v204, v200
	v_max_f32_e32 v0, v0, v0
	v_max_f32_e32 v0, v0, v52
	s_waitcnt lgkmcnt(2)
	v_mfma_f32_32x32x64_f8f6f4 v[4:19], v[60:67], v[132:139], v[4:19]
	v_exp_f32_e32 v161, v84
	v_exp_f32_e32 v163, v85
	v_exp_f32_e32 v162, v86
	v_exp_f32_e32 v164, v87
	v_exp_f32_e32 v150, v88
	v_exp_f32_e32 v154, v89
	v_exp_f32_e32 v152, v90
	v_exp_f32_e32 v157, v91
	v_add_u32_e32 v141, s15, v176
	ds_read_b128 v[84:87], v141
	ds_read_b128 v[88:91], v141 offset:1024
	v_mfma_f32_16x16x128_f8f6f4 v[200:203], v[124:131], v[132:139], v[200:203]
	v_exp_f32_e32 v149, v92
	v_exp_f32_e32 v153, v93
	v_exp_f32_e32 v151, v94
	v_exp_f32_e32 v156, v95
	v_exp_f32_e32 v155, v96
	v_exp_f32_e32 v159, v97
	v_exp_f32_e32 v158, v98
	v_exp_f32_e32 v160, v99
	ds_read_b128 v[92:95], v141 offset:512
	ds_read_b128 v[96:99], v141 offset:1536
	s_waitcnt lgkmcnt(4)
	v_mfma_f32_32x32x64_f8f6f4 v[20:35], v[178:185], v[132:139], v[20:35]
	v_exp_f32_e32 v100, v100
	v_exp_f32_e32 v148, v101
	v_exp_f32_e32 v101, v102
	v_exp_f32_e32 v102, v103
	v_exp_f32_e32 v143, v104
	v_exp_f32_e32 v146, v105
	v_exp_f32_e32 v145, v106
	v_exp_f32_e32 v147, v107
	v_exp_f32_e32 v69, v108
	v_exp_f32_e32 v109, v109
	v_exp_f32_e32 v108, v110
	v_exp_f32_e32 v142, v111
	v_exp_f32_e32 v110, v112
	v_exp_f32_e32 v144, v113
	v_exp_f32_e32 v111, v114
	v_exp_f32_e32 v114, v115
	s_add_i32 s16, s15, 0x4000
	s_cmpk_lg_u32 s15, 0x8000
	s_mov_b32 s36, s13
	s_mov_b32 s14, s15
	s_cselect_b32 s13, s16, 0
	s_add_i32 s12, s12, 2
	s_cmp_gt_u32 s12, 26
	s_waitcnt vmcnt(2) lgkmcnt(0)
	s_barrier
	s_cbranch_scc0 .LBB1_1
	s_and_b32 s41, s2, 3
	s_lshl_b32 s42, s41, 6
	s_lshl_b32 s43, s3, 5
	s_add_i32 s42, s42, s43
	v_add_u32_e32 v198, s42, v172
	v_lshlrev_b32_e32 v198, 8, v198
	v_lshl_add_u32 v198, v175, 4, v198
	s_lshl_b32 s44, s41, 8
	s_lshl_b32 s45, s3, 7
	s_add_i32 s44, s44, s45
	v_lshl_add_u32 v199, v175, 4, s44
	s_lshl_b32 s46, s41, 2
	v_mov_b32_e32 v205, s46
	v_add_u32_e32 v113, 0xc000, v176
	v_mov_b32_e32 v112, 0x7f7f7f7f
	v_cvt_pk_fp8_f32 v132, v161, v163
	v_cvt_pk_fp8_f32 v132, v162, v164 op_sel:[0,0,1]
	s_waitcnt lgkmcnt(2)
	v_mfma_f32_32x32x64_f8f6f4 v[70:85], v[84:91], v[116:123], v[36:51]
	ds_read_b128 v[162:165], v113 offset:32768
	ds_read_b128 v[166:169], v113 offset:33792
	v_cvt_pk_fp8_f32 v133, v150, v154
	v_cvt_pk_fp8_f32 v133, v152, v157 op_sel:[0,0,1]
	s_mov_b32 s13, 0x1e000
	s_mov_b32 m0, s33
	s_nop 0
	buffer_load_dwordx4 v174, s[20:23], s13 offen lds
	v_cvt_pk_fp8_f32 v134, v149, v153
	v_cvt_pk_fp8_f32 v134, v151, v156 op_sel:[0,0,1]
	v_cvt_pk_fp8_f32 v135, v155, v159
	v_cvt_pk_fp8_f32 v135, v158, v160 op_sel:[0,0,1]
	v_cvt_pk_fp8_f32 v136, v100, v148
	v_cvt_pk_fp8_f32 v136, v101, v102 op_sel:[0,0,1]
	s_waitcnt lgkmcnt(2)
	v_mfma_f32_32x32x64_f8f6f4 v[86:101], v[92:99], v[116:123], v[36:51]
	ds_read_b128 v[148:151], v113 offset:33280
	ds_read_b128 v[152:155], v113 offset:34304
	v_cvt_pk_fp8_f32 v137, v143, v146
	v_cvt_pk_fp8_f32 v137, v145, v147 op_sel:[0,0,1]
	s_cmp_lg_u32 0, -1
	s_cselect_b32 s12, 0, 0
	s_add_i32 s15, s12, s35
	s_add_i32 s12, s15, 0x10000
	s_mov_b32 s26, s22
	s_mov_b32 s27, s23
	s_mov_b32 s14, 0x1c000
	s_mov_b32 m0, s12
	s_nop 0
	buffer_load_dwordx4 v174, s[24:27], s14 offen lds
	global_load_dwordx4 v[208:211], v198, s[4:5]
	global_load_dwordx4 v[212:215], v198, s[4:5] offset:32
	global_load_dwordx4 v[216:219], v198, s[4:5] offset:64
	global_load_dwordx4 v[220:223], v198, s[4:5] offset:96
	global_load_dwordx4 v[224:227], v198, s[4:5] offset:128
	v_cvt_pk_fp8_f32 v138, v69, v109
	v_cvt_pk_fp8_f32 v138, v108, v142 op_sel:[0,0,1]
	v_cvt_pk_fp8_f32 v139, v110, v144
	v_cvt_pk_fp8_f32 v139, v111, v114 op_sel:[0,0,1]
	s_waitcnt lgkmcnt(2)
	s_nop 0
	v_mfma_f32_32x32x64_f8f6f4 v[4:19], v[162:169], v[132:139], v[4:19]
	v_exp_f32_e32 v104, v73
	v_exp_f32_e32 v69, v70
	v_exp_f32_e32 v102, v71
	v_exp_f32_e32 v103, v72
	v_exp_f32_e32 v110, v74
	v_exp_f32_e32 v111, v75
	v_exp_f32_e32 v114, v76
	v_exp_f32_e32 v115, v77
	ds_read_b128 v[70:73], v176 offset:16384
	ds_read_b128 v[74:77], v176 offset:17408
	v_mfma_f32_16x16x128_f8f6f4 v[200:203], v[124:131], v[132:139], v[200:203]
	v_exp_f32_e32 v140, v78
	v_exp_f32_e32 v141, v79
	v_exp_f32_e32 v142, v80
	v_exp_f32_e32 v143, v81
	v_exp_f32_e32 v144, v82
	v_exp_f32_e32 v145, v83
	v_exp_f32_e32 v146, v84
	v_exp_f32_e32 v147, v85
	s_waitcnt lgkmcnt(2)
	v_mfma_f32_32x32x64_f8f6f4 v[20:35], v[148:155], v[132:139], v[20:35]
	v_exp_f32_e32 v156, v86
	v_exp_f32_e32 v157, v87
	v_exp_f32_e32 v158, v88
	v_exp_f32_e32 v159, v89
	v_exp_f32_e32 v148, v90
	v_exp_f32_e32 v149, v91
	v_exp_f32_e32 v150, v92
	v_exp_f32_e32 v151, v93
	ds_read_b128 v[86:89], v176 offset:16896
	ds_read_b128 v[90:93], v176 offset:17920
	v_exp_f32_e32 v152, v94
	v_exp_f32_e32 v153, v95
	v_exp_f32_e32 v154, v96
	v_exp_f32_e32 v155, v97
	v_exp_f32_e32 v160, v98
	v_exp_f32_e32 v161, v99
	v_exp_f32_e32 v162, v100
	v_exp_f32_e32 v163, v101
	s_waitcnt vmcnt(7) lgkmcnt(0)
	s_barrier
	s_waitcnt lgkmcnt(2)
	v_mfma_f32_32x32x64_f8f6f4 v[70:85], v[70:77], v[116:123], v[36:51]
	v_cvt_pk_fp8_f32 v132, v69, v102
	v_cvt_pk_fp8_f32 v132, v103, v104 op_sel:[0,0,1]
	ds_read_b128 v[102:105], v176 offset:49152
	ds_read_b128 v[106:109], v176 offset:50176
	v_cvt_pk_fp8_f32 v133, v110, v111
	v_cvt_pk_fp8_f32 v133, v114, v115 op_sel:[0,0,1]
	s_add_i32 s16, s15, 0x4000
	s_mov_b32 s14, 0x1f000
	s_mov_b32 m0, s16
	s_nop 0
	buffer_load_dwordx4 v174, s[20:23], s14 offen lds
	v_cvt_pk_fp8_f32 v134, v140, v141
	v_cvt_pk_fp8_f32 v134, v142, v143 op_sel:[0,0,1]
	v_cvt_pk_fp8_f32 v135, v144, v145
	v_cvt_pk_fp8_f32 v135, v146, v147 op_sel:[0,0,1]
	s_waitcnt lgkmcnt(2)
	v_mfma_f32_32x32x64_f8f6f4 v[86:101], v[86:93], v[116:123], v[36:51]
	v_cvt_pk_fp8_f32 v136, v156, v157
	v_cvt_pk_fp8_f32 v136, v158, v159 op_sel:[0,0,1]
	ds_read_b128 v[140:143], v176 offset:49664
	ds_read_b128 v[144:147], v176 offset:50688
	v_cvt_pk_fp8_f32 v137, v148, v149
	v_cvt_pk_fp8_f32 v137, v150, v151 op_sel:[0,0,1]
	s_add_i32 s15, s15, 0x14000
	s_mov_b32 s16, 0x1d000
	s_mov_b32 m0, s15
	s_nop 0
	buffer_load_dwordx4 v174, s[24:27], s16 offen lds
	global_load_dwordx4 v[228:231], v198, s[4:5] offset:160
	global_load_dwordx4 v[232:235], v198, s[4:5] offset:192
	global_load_dwordx4 v[236:239], v198, s[4:5] offset:224
	global_load_dwordx4 v[240:243], v199, s[6:7]
	v_cvt_pk_fp8_f32 v138, v152, v153
	v_cvt_pk_fp8_f32 v138, v154, v155 op_sel:[0,0,1]
	v_cvt_pk_fp8_f32 v139, v160, v161
	v_cvt_pk_fp8_f32 v139, v162, v163 op_sel:[0,0,1]
	v_sub_f32_e32 v114, v200, v204
	v_mov_b32_e32 v204, v200
	s_waitcnt lgkmcnt(2)
	v_mfma_f32_32x32x64_f8f6f4 v[4:19], v[102:109], v[132:139], v[4:19]
	v_exp_f32_e32 v110, v70
	v_exp_f32_e32 v111, v71
	v_exp_f32_e32 v148, v73
	v_exp_f32_e32 v115, v72
	v_exp_f32_e32 v149, v74
	v_exp_f32_e32 v150, v75
	v_exp_f32_e32 v151, v76
	v_exp_f32_e32 v152, v77
	ds_read_b128 v[70:73], v176 offset:32768
	ds_read_b128 v[74:77], v176 offset:33792
	v_mfma_f32_16x16x128_f8f6f4 v[200:203], v[124:131], v[132:139], v[200:203]
	v_exp_f32_e32 v153, v78
	v_exp_f32_e32 v154, v79
	v_exp_f32_e32 v155, v80
	v_exp_f32_e32 v156, v81
	v_exp_f32_e32 v157, v83
	v_exp_f32_e32 v158, v84
	v_exp_f32_e32 v159, v85
	v_exp_f32_e32 v53, v82
	s_waitcnt lgkmcnt(2)
	v_mfma_f32_32x32x64_f8f6f4 v[20:35], v[140:147], v[132:139], v[20:35]
	v_exp_f32_e32 v160, v86
	v_exp_f32_e32 v161, v87
	v_exp_f32_e32 v162, v88
	v_exp_f32_e32 v163, v89
	v_exp_f32_e32 v164, v90
	v_exp_f32_e32 v165, v91
	v_exp_f32_e32 v166, v92
	v_exp_f32_e32 v167, v93
	ds_read_b128 v[78:81], v176 offset:33280
	ds_read_b128 v[82:85], v176 offset:34304
	v_exp_f32_e32 v168, v94
	v_exp_f32_e32 v169, v95
	v_exp_f32_e32 v170, v96
	v_exp_f32_e32 v171, v97
	v_exp_f32_e32 v177, v98
	v_exp_f32_e32 v178, v99
	v_exp_f32_e32 v179, v100
	v_exp_f32_e32 v180, v101
	s_waitcnt vmcnt(11) lgkmcnt(0)
	s_barrier
	s_waitcnt lgkmcnt(2)
	v_mfma_f32_32x32x64_f8f6f4 v[86:101], v[70:77], v[116:123], v[36:51]
	v_cvt_pk_fp8_f32 v132, v110, v111
	v_cvt_pk_fp8_f32 v132, v115, v148 op_sel:[0,0,1]
	ds_read_b128 v[102:105], v113 offset:16384
	ds_read_b128 v[106:109], v113 offset:17408
	v_cvt_pk_fp8_f32 v133, v149, v150
	v_cvt_pk_fp8_f32 v133, v151, v152 op_sel:[0,0,1]
	v_cvt_pk_fp8_f32 v134, v153, v154
	v_cvt_pk_fp8_f32 v134, v155, v156 op_sel:[0,0,1]
	v_cvt_pk_fp8_f32 v135, v53, v157
	v_cvt_pk_fp8_f32 v135, v158, v159 op_sel:[0,0,1]
	s_waitcnt lgkmcnt(2)
	v_mfma_f32_32x32x64_f8f6f4 v[70:85], v[78:85], v[116:123], v[36:51]
	v_cvt_pk_fp8_f32 v136, v160, v161
	v_cvt_pk_fp8_f32 v136, v162, v163 op_sel:[0,0,1]
	ds_read_b128 v[140:143], v113 offset:16896
	ds_read_b128 v[144:147], v113 offset:17920
	v_cvt_pk_fp8_f32 v137, v164, v165
	v_cvt_pk_fp8_f32 v137, v166, v167 op_sel:[0,0,1]
	s_mov_b32 m0, s34
	s_nop 0
	buffer_load_dwordx4 v174, s[24:27], s13 offen lds
	global_load_dwordx4 v[244:247], v199, s[6:7] offset:32
	global_load_dwordx4 v[248:251], v199, s[6:7] offset:64
	global_load_dwordx4 v[252:255], v199, s[6:7] offset:96
	global_load_dword v205, v205, s[8:9]
	v_cvt_pk_fp8_f32 v138, v168, v169
	v_cvt_pk_fp8_f32 v138, v170, v171 op_sel:[0,0,1]
	v_cvt_pk_fp8_f32 v139, v177, v178
	v_cvt_pk_fp8_f32 v139, v179, v180 op_sel:[0,0,1]
	s_waitcnt lgkmcnt(2)
	s_nop 0
	v_mfma_f32_32x32x64_f8f6f4 v[4:19], v[102:109], v[132:139], v[4:19]
	v_exp_f32_e32 v148, v88
	v_exp_f32_e32 v149, v89
	v_exp_f32_e32 v53, v86
	v_exp_f32_e32 v115, v87
	v_exp_f32_e32 v150, v92
	v_exp_f32_e32 v151, v93
	v_exp_f32_e32 v102, v90
	v_exp_f32_e32 v103, v91
	ds_read_b128 v[86:89], v176
	ds_read_b128 v[90:93], v176 offset:1024
	v_mfma_f32_16x16x128_f8f6f4 v[200:203], v[124:131], v[132:139], v[200:203]
	v_exp_f32_e32 v152, v94
	v_exp_f32_e32 v153, v95
	v_exp_f32_e32 v154, v96
	v_exp_f32_e32 v155, v97
	v_exp_f32_e32 v156, v98
	v_exp_f32_e32 v157, v99
	v_exp_f32_e32 v158, v100
	v_exp_f32_e32 v159, v101
	s_waitcnt lgkmcnt(2)
	v_mfma_f32_32x32x64_f8f6f4 v[20:35], v[140:147], v[132:139], v[20:35]
	v_exp_f32_e32 v160, v70
	v_exp_f32_e32 v161, v71
	v_exp_f32_e32 v162, v72
	v_exp_f32_e32 v163, v73
	v_exp_f32_e32 v164, v74
	v_exp_f32_e32 v165, v75
	v_exp_f32_e32 v166, v76
	v_exp_f32_e32 v167, v77
	ds_read_b128 v[94:97], v176 offset:512
	ds_read_b128 v[98:101], v176 offset:1536
	v_exp_f32_e32 v168, v78
	v_exp_f32_e32 v169, v79
	v_exp_f32_e32 v170, v80
	v_exp_f32_e32 v171, v81
	v_exp_f32_e32 v177, v82
	v_exp_f32_e32 v178, v83
	v_exp_f32_e32 v179, v84
	v_exp_f32_e32 v180, v85
	s_waitcnt vmcnt(9) lgkmcnt(0)
	s_barrier
	s_waitcnt lgkmcnt(2)
	v_mfma_f32_32x32x64_f8f6f4 v[70:85], v[86:93], v[116:123], v[36:51]
	ds_read_b128 v[104:107], v113 offset:32768
	ds_read_b128 v[108:111], v113 offset:33792
	v_cvt_pk_fp8_f32 v132, v53, v115
	v_cvt_pk_fp8_f32 v133, v102, v103
	v_cvt_pk_fp8_f32 v134, v152, v153
	v_cvt_pk_fp8_f32 v132, v148, v149 op_sel:[0,0,1]
	v_cvt_pk_fp8_f32 v133, v150, v151 op_sel:[0,0,1]
	v_cvt_pk_fp8_f32 v134, v154, v155 op_sel:[0,0,1]
	v_cvt_pk_fp8_f32 v135, v156, v157
	v_cvt_pk_fp8_f32 v135, v158, v159 op_sel:[0,0,1]
	s_waitcnt lgkmcnt(2)
	v_mfma_f32_32x32x64_f8f6f4 v[86:101], v[94:101], v[116:123], v[36:51]
	v_cvt_pk_fp8_f32 v136, v160, v161
	v_cvt_pk_fp8_f32 v136, v162, v163 op_sel:[0,0,1]
	ds_read_b128 v[140:143], v113 offset:33280
	ds_read_b128 v[144:147], v113 offset:34304
	v_cvt_pk_fp8_f32 v137, v164, v165
	v_cvt_pk_fp8_f32 v137, v166, v167 op_sel:[0,0,1]
	s_mov_b32 m0, s12
	s_nop 0
	buffer_load_dwordx4 v174, s[24:27], s14 offen lds
	v_cvt_pk_fp8_f32 v138, v168, v169
	v_cvt_pk_fp8_f32 v138, v170, v171 op_sel:[0,0,1]
	v_cvt_pk_fp8_f32 v139, v177, v178
	v_cvt_pk_fp8_f32 v139, v179, v180 op_sel:[0,0,1]
	v_sub_f32_e32 v52, v200, v204
	v_mov_b32_e32 v204, v200
	v_max3_f32 v0, v0, v114, v52
	v_exp_f32_e32 v72, v72
	v_exp_f32_e32 v73, v73
	v_exp_f32_e32 v52, v70
	v_exp_f32_e32 v53, v71
	v_exp_f32_e32 v102, v74
	v_exp_f32_e32 v103, v75
	v_exp_f32_e32 v114, v76
	v_exp_f32_e32 v115, v77
	ds_read_b128 v[150:153], v176 offset:16384
	ds_read_b128 v[154:157], v176 offset:17408
	v_mfma_f32_16x16x128_f8f6f4 v[200:203], v[124:131], v[132:139], v[200:203]
	v_exp_f32_e32 v177, v78
	v_exp_f32_e32 v178, v79
	v_exp_f32_e32 v179, v80
	v_exp_f32_e32 v180, v81
	v_exp_f32_e32 v55, v82
	v_exp_f32_e32 v181, v83
	v_exp_f32_e32 v182, v84
	v_exp_f32_e32 v183, v85
	v_exp_f32_e32 v184, v86
	v_exp_f32_e32 v185, v87
	v_exp_f32_e32 v88, v88
	v_exp_f32_e32 v89, v89
	v_exp_f32_e32 v186, v90
	v_exp_f32_e32 v187, v91
	v_exp_f32_e32 v188, v92
	v_exp_f32_e32 v189, v93
	ds_read_b128 v[164:167], v176 offset:16896
	ds_read_b128 v[168:171], v176 offset:17920
	v_exp_f32_e32 v190, v94
	v_exp_f32_e32 v191, v95
	v_exp_f32_e32 v192, v96
	v_exp_f32_e32 v193, v97
	v_exp_f32_e32 v194, v98
	v_exp_f32_e32 v195, v99
	v_exp_f32_e32 v196, v100
	v_exp_f32_e32 v197, v101
	s_waitcnt vmcnt(0) lgkmcnt(0)
	s_barrier
	v_mov_b32_e32 v148, v132
	v_cvt_pk_fp8_f32 v148, v52, v53
	v_cvt_pk_fp8_f32 v148, v72, v73 op_sel:[0,0,1]
	s_waitcnt lgkmcnt(2)
	v_mfma_f32_32x32x64_f8f6f4 v[72:87], v[150:157], v[116:123], v[36:51]
	ds_read_b128 v[156:159], v176 offset:49152
	ds_read_b128 v[160:163], v176 offset:50176
	v_mov_b32_e32 v149, v133
	v_cvt_pk_fp8_f32 v149, v102, v103
	v_cvt_pk_fp8_f32 v149, v114, v115 op_sel:[0,0,1]
	v_mov_b32_e32 v150, v134
	v_cvt_pk_fp8_f32 v150, v177, v178
	v_cvt_pk_fp8_f32 v150, v179, v180 op_sel:[0,0,1]
	v_mov_b32_e32 v151, v135
	v_cvt_pk_fp8_f32 v151, v55, v181
	v_cvt_pk_fp8_f32 v151, v182, v183 op_sel:[0,0,1]
	v_mov_b32_e32 v152, v136
	v_cvt_pk_fp8_f32 v152, v184, v185
	v_cvt_pk_fp8_f32 v152, v88, v89 op_sel:[0,0,1]
	s_waitcnt lgkmcnt(2)
	v_mfma_f32_32x32x64_f8f6f4 v[88:103], v[164:171], v[116:123], v[36:51]
	ds_read_b128 v[164:167], v176 offset:49664
	ds_read_b128 v[168:171], v176 offset:50688
	v_mov_b32_e32 v153, v137
	v_cvt_pk_fp8_f32 v153, v186, v187
	v_cvt_pk_fp8_f32 v153, v188, v189 op_sel:[0,0,1]
	v_mov_b32_e32 v154, v138
	v_cvt_pk_fp8_f32 v154, v190, v191
	v_cvt_pk_fp8_f32 v154, v192, v193 op_sel:[0,0,1]
	v_mov_b32_e32 v155, v139
	v_cvt_pk_fp8_f32 v155, v194, v195
	v_cvt_pk_fp8_f32 v155, v196, v197 op_sel:[0,0,1]
	v_sub_f32_e32 v52, v200, v204
	v_mov_b32_e32 v204, v200
	s_nop 2
	v_exp_f32_e32 v36, v72
	v_exp_f32_e32 v37, v73
	v_exp_f32_e32 v38, v74
	v_exp_f32_e32 v39, v75
	v_exp_f32_e32 v40, v76
	v_exp_f32_e32 v41, v77
	v_exp_f32_e32 v42, v78
	v_exp_f32_e32 v43, v79
	v_exp_f32_e32 v53, v80
	v_exp_f32_e32 v80, v83
	v_exp_f32_e32 v54, v81
	v_exp_f32_e32 v55, v82
	v_exp_f32_e32 v81, v84
	v_exp_f32_e32 v82, v85
	v_exp_f32_e32 v83, v86
	v_exp_f32_e32 v84, v87
	v_exp_f32_e32 v44, v88
	v_exp_f32_e32 v45, v89
	v_exp_f32_e32 v46, v90
	v_exp_f32_e32 v47, v91
	v_exp_f32_e32 v48, v92
	v_exp_f32_e32 v49, v93
	v_exp_f32_e32 v50, v94
	v_exp_f32_e32 v51, v95
	v_exp_f32_e32 v75, v96
	v_exp_f32_e32 v85, v97
	v_exp_f32_e32 v86, v98
	v_exp_f32_e32 v87, v99
	v_exp_f32_e32 v88, v100
	v_exp_f32_e32 v89, v101
	v_exp_f32_e32 v90, v102
	v_exp_f32_e32 v91, v103
	v_mov_b32_e32 v72, 0
	v_mov_b32_e32 v76, 0
	v_mov_b32_e32 v73, 0
	v_mov_b32_e32 v77, 0
	v_cvt_pk_fp8_f32 v72, v36, v37
	v_cvt_pk_fp8_f32 v76, v44, v45
	v_cvt_pk_fp8_f32 v73, v40, v41
	v_cvt_pk_fp8_f32 v77, v48, v49
	v_cvt_pk_fp8_f32 v72, v38, v39 op_sel:[0,0,1]
	v_cvt_pk_fp8_f32 v76, v46, v47 op_sel:[0,0,1]
	v_cvt_pk_fp8_f32 v73, v42, v43 op_sel:[0,0,1]
	v_cvt_pk_fp8_f32 v77, v50, v51 op_sel:[0,0,1]
	v_mfma_f32_16x16x128_f8f6f4 v[200:203], v[124:131], v[148:155], v[200:203]
	v_mov_b32_e32 v78, 0
	v_mov_b32_e32 v79, 0
	v_mov_b32_e32 v74, 0
	v_cvt_pk_fp8_f32 v78, v75, v85
	v_mov_b32_e32 v75, 0
	v_cvt_pk_fp8_f32 v74, v53, v54
	v_cvt_pk_fp8_f32 v75, v81, v82
	v_cvt_pk_fp8_f32 v79, v88, v89
	v_cvt_pk_fp8_f32 v78, v86, v87 op_sel:[0,0,1]
	v_cvt_pk_fp8_f32 v74, v55, v80 op_sel:[0,0,1]
	v_cvt_pk_fp8_f32 v75, v83, v84 op_sel:[0,0,1]
	v_cvt_pk_fp8_f32 v79, v90, v91 op_sel:[0,0,1]
	ds_read_b128 v[80:83], v113 offset:16384
	s_nop 1
	ds_read_b128 v[58:61], v113 offset:16896
	ds_read_b128 v[84:87], v113 offset:17408
	ds_read_b128 v[62:65], v113 offset:17920
	s_mov_b32 s12, 0x43c80000
	v_mfma_f32_16x16x128_f8f6f4 v[200:203], v[124:131], v[72:79], v[200:203]
	s_nop 15
	s_nop 3
	v_sub_f32_e32 v37, v200, v204
	v_max3_f32 v0, v0, v52, v37
	v_cmp_nge_f32_e32 vcc, s12, v0
	s_cmp_lg_u64 vcc, 0
	s_cselect_b64 s[12:13], -1, 0
	s_cbranch_vccz .LBB1_12
	v_mfma_f32_32x32x64_f8f6f4 v[4:19], v[104:111], v[132:139], v[4:19]
	s_andn2_b64 vcc, exec, s[12:13]
	v_mfma_f32_32x32x64_f8f6f4 v[20:35], v[140:147], v[132:139], v[20:35]
	s_cbranch_vccnz .LBB1_5

.LBB1_11:
	s_lshl_b32 s0, s30, 5
	s_lshl_b32 s1, s31, 7
	s_and_b32 s13, s2, 3
	s_or_b32 s14, s0, s1
	s_lshl_b32 s4, s28, 7
	s_lshl_b32 s5, s31, 2
	s_add_i32 s4, s4, s5
	s_add_i32 s4, s4, s30
	s_lshl_b32 s4, s4, 1
	s_add_i32 s4, s4, s3
	s_lshl_b32 s4, s4, 12
	s_add_u32 s4, s18, s4
	s_addc_u32 s5, s19, 0
	v_lshlrev_b32_e32 v0, 2, v173
	s_lshl_b32 s0, s3, 5
	s_lshl_b32 s12, s13, 6
	s_mov_b32 s1, 0
	s_mov_b32 s15, 0
	global_load_dwordx4 v[124:127], v0, s[4:5]
	global_load_dwordx4 v[128:131], v0, s[4:5] offset:1024
	global_load_dwordx4 v[132:135], v0, s[4:5] offset:2048
	global_load_dwordx4 v[136:139], v0, s[4:5] offset:3072
	s_lshl_b64 s[2:3], s[14:15], 2
	v_mov_b32_e32 v37, 0
	v_lshlrev_b32_e32 v36, 2, v172
	v_lshlrev_b32_e32 v122, 16, v175
	v_mov_b32_e32 v123, 0
	s_mul_i32 s4, s29, 0x2200
	s_add_i32 s4, s4, 0
	v_mov_b32_e32 v8, v141
	v_add_u32_e32 v9, s4, v173
	s_xor_b32 s4, s29, 4
	v_permlane32_swap_b32_e32 v141, v8
	s_mulk_i32 s4, 0x2200
	v_add_f32_e32 v8, v141, v8
	s_add_i32 s4, s4, 0
	ds_write2st64_b32 v9, v146, v8 offset1:1
	ds_write2st64_b32 v9, v54, v55 offset0:2 offset1:3
	ds_write2st64_b32 v9, v38, v39 offset0:18 offset1:19
	ds_write2st64_b32 v9, v56, v57 offset0:4 offset1:5
	ds_write2st64_b32 v9, v40, v41 offset0:20 offset1:21
	ds_write2st64_b32 v9, v58, v59 offset0:6 offset1:7
	ds_write2st64_b32 v9, v42, v43 offset0:22 offset1:23
	ds_write2st64_b32 v9, v60, v61 offset0:8 offset1:9
	ds_write2st64_b32 v9, v44, v45 offset0:24 offset1:25
	ds_write2st64_b32 v9, v62, v63 offset0:10 offset1:11
	ds_write2st64_b32 v9, v46, v47 offset0:26 offset1:27
	ds_write2st64_b32 v9, v64, v65 offset0:12 offset1:13
	ds_write2st64_b32 v9, v48, v49 offset0:28 offset1:29
	ds_write2st64_b32 v9, v66, v67 offset0:14 offset1:15
	ds_write2st64_b32 v9, v50, v51 offset0:30 offset1:31
	ds_write2st64_b32 v9, v68, v69 offset0:16 offset1:17
	ds_write2st64_b32 v9, v52, v53 offset0:32 offset1:33
	v_add_u32_e32 v66, s4, v173
	s_waitcnt lgkmcnt(0)
	s_barrier
	ds_read2st64_b32 v[10:11], v66 offset1:1
	ds_read2st64_b32 v[12:13], v66 offset0:2 offset1:3
	ds_read2st64_b32 v[14:15], v66 offset0:4 offset1:5
	ds_read2st64_b32 v[38:39], v66 offset0:6 offset1:7
	v_max_f32_e32 v40, v146, v146
	s_waitcnt lgkmcnt(3)
	v_max_f32_e32 v9, v10, v10
	v_max_f32_e32 v9, v40, v9
	v_sub_f32_e32 v40, v146, v9
	v_sub_f32_e32 v9, v10, v9
	v_exp_f32_e32 v40, v40
	v_exp_f32_e32 v41, v9
	v_mov_b32_e32 v9, v11
	v_pk_mul_f32 v[8:9], v[8:9], v[40:41]
	s_nop 0
	v_add_f32_e32 v8, v8, v9
	v_div_scale_f32 v9, s[4:5], v8, v8, 1.0
	v_rcp_f32_e32 v10, v9
	s_nop 0
	v_fma_f32 v11, -v9, v10, 1.0
	v_fmac_f32_e32 v10, v11, v10
	v_div_scale_f32 v11, vcc, 1.0, v8, 1.0
	v_mul_f32_e32 v42, v11, v10
	v_fma_f32 v43, -v9, v42, v11
	v_fmac_f32_e32 v42, v43, v10
	v_fma_f32 v9, -v9, v42, v11
	v_div_fmas_f32 v9, v9, v10, v42
	v_div_fixup_f32 v9, v9, v8, 1.0
	v_mul_f32_e32 v8, v40, v9
	v_mul_f32_e32 v10, v41, v9
	ds_read2st64_b32 v[40:41], v66 offset0:18 offset1:19
	ds_read2st64_b32 v[42:43], v66 offset0:20 offset1:21
	ds_read2st64_b32 v[44:45], v66 offset0:22 offset1:23
	ds_read2st64_b32 v[46:47], v66 offset0:16 offset1:17
	s_waitcnt lgkmcnt(6)
	v_pk_mul_f32 v[12:13], v[10:11], v[12:13] op_sel_hi:[0,1]
	s_waitcnt lgkmcnt(5)
	v_pk_mul_f32 v[14:15], v[10:11], v[14:15] op_sel_hi:[0,1]
	s_waitcnt lgkmcnt(4)
	v_pk_mul_f32 v[38:39], v[10:11], v[38:39] op_sel_hi:[0,1]
	s_waitcnt lgkmcnt(3)
	v_pk_mul_f32 v[40:41], v[10:11], v[40:41] op_sel_hi:[0,1]
	v_pk_fma_f32 v[48:49], v[8:9], v[70:71], v[40:41] op_sel_hi:[0,1,1]
	s_waitcnt lgkmcnt(2)
	v_pk_mul_f32 v[40:41], v[10:11], v[42:43] op_sel_hi:[0,1]
	v_pk_fma_f32 v[50:51], v[8:9], v[72:73], v[40:41] op_sel_hi:[0,1,1]
	s_waitcnt lgkmcnt(1)
	v_pk_mul_f32 v[40:41], v[10:11], v[44:45] op_sel_hi:[0,1]
	v_pk_fma_f32 v[52:53], v[8:9], v[74:75], v[40:41] op_sel_hi:[0,1,1]
	ds_read2st64_b32 v[40:41], v66 offset0:8 offset1:9
	ds_read2st64_b32 v[42:43], v66 offset0:24 offset1:25
	ds_read2st64_b32 v[44:45], v66 offset0:10 offset1:11
	ds_read2st64_b32 v[54:55], v66 offset0:12 offset1:13
	ds_read2st64_b32 v[56:57], v66 offset0:14 offset1:15
	ds_read2st64_b32 v[58:59], v66 offset0:26 offset1:27
	ds_read2st64_b32 v[60:61], v66 offset0:28 offset1:29
	ds_read2st64_b32 v[62:63], v66 offset0:30 offset1:31
	s_waitcnt lgkmcnt(6)
	v_pk_mul_f32 v[42:43], v[10:11], v[42:43] op_sel_hi:[0,1]
	v_pk_fma_f32 v[64:65], v[8:9], v[76:77], v[42:43] op_sel_hi:[0,1,1]
	s_waitcnt lgkmcnt(5)
	v_pk_mul_f32 v[42:43], v[10:11], v[44:45] op_sel_hi:[0,1]
	s_waitcnt lgkmcnt(2)
	v_pk_mul_f32 v[44:45], v[10:11], v[58:59] op_sel_hi:[0,1]
	v_pk_fma_f32 v[58:59], v[8:9], v[78:79], v[44:45] op_sel_hi:[0,1,1]
	v_pk_mul_f32 v[44:45], v[10:11], v[54:55] op_sel_hi:[0,1]
	s_waitcnt lgkmcnt(1)
	v_pk_mul_f32 v[54:55], v[10:11], v[60:61] op_sel_hi:[0,1]
	ds_read2st64_b32 v[60:61], v66 offset0:32 offset1:33
	s_waitcnt vmcnt(4)
	v_pk_mul_f32 v[40:41], v[10:11], v[40:41] op_sel_hi:[0,1]
	v_cvt_pk_bf16_f32 v0, v208, v209
	v_cvt_pk_bf16_f32 v1, v210, v211
	v_cvt_pk_bf16_f32 v2, v212, v213
	v_cvt_pk_bf16_f32 v3, v214, v215
	v_pk_fma_f32 v[12:13], v[8:9], v[86:87], v[12:13] op_sel_hi:[0,1,1]
	v_pk_fma_f32 v[14:15], v[8:9], v[88:89], v[14:15] op_sel_hi:[0,1,1]
	v_pk_fma_f32 v[38:39], v[8:9], v[90:91], v[38:39] op_sel_hi:[0,1,1]
	v_pk_fma_f32 v[40:41], v[8:9], v[92:93], v[40:41] op_sel_hi:[0,1,1]
	v_pk_mul_f32 v[56:57], v[10:11], v[56:57] op_sel_hi:[0,1]
	s_waitcnt lgkmcnt(1)
	v_pk_mul_f32 v[62:63], v[10:11], v[62:63] op_sel_hi:[0,1]
	v_pk_mul_f32 v[46:47], v[10:11], v[46:47] op_sel_hi:[0,1]
	s_waitcnt lgkmcnt(0)
	v_pk_mul_f32 v[10:11], v[10:11], v[60:61] op_sel_hi:[0,1]
	v_cvt_pk_bf16_f32 v4, v12, v13
	v_cvt_pk_bf16_f32 v5, v14, v15
	v_cvt_pk_bf16_f32 v6, v38, v39
	v_cvt_pk_bf16_f32 v7, v40, v41
	v_pk_fma_f32 v[42:43], v[8:9], v[94:95], v[42:43] op_sel_hi:[0,1,1]
	v_pk_fma_f32 v[44:45], v[8:9], v[96:97], v[44:45] op_sel_hi:[0,1,1]
	v_pk_fma_f32 v[54:55], v[8:9], v[80:81], v[54:55] op_sel_hi:[0,1,1]
	v_pk_fma_f32 v[56:57], v[8:9], v[98:99], v[56:57] op_sel_hi:[0,1,1]
	v_pk_fma_f32 v[62:63], v[8:9], v[82:83], v[62:63] op_sel_hi:[0,1,1]
	v_pk_fma_f32 v[46:47], v[8:9], v[100:101], v[46:47] op_sel_hi:[0,1,1]
	v_pk_fma_f32 v[60:61], v[8:9], v[84:85], v[10:11] op_sel_hi:[0,1,1]
	v_mfma_f32_32x32x16_bf16 v[0:15], v[0:3], v[4:7], 0
	v_cvt_pk_bf16_f32 v42, v42, v43
	v_cvt_pk_bf16_f32 v38, v216, v217
	v_cvt_pk_bf16_f32 v39, v218, v219
	v_cvt_pk_bf16_f32 v40, v220, v221
	v_cvt_pk_bf16_f32 v41, v222, v223
	v_cvt_pk_bf16_f32 v43, v44, v45
	v_cvt_pk_bf16_f32 v44, v56, v57
	v_cvt_pk_bf16_f32 v45, v46, v47
	s_nop 1
	v_mfma_f32_32x32x16_bf16 v[0:15], v[38:41], v[42:45], v[0:15]
	v_cvt_pk_bf16_f32 v38, v224, v225
	v_cvt_pk_bf16_f32 v39, v226, v227
	v_cvt_pk_bf16_f32 v40, v228, v229
	v_cvt_pk_bf16_f32 v41, v230, v231
	v_cvt_pk_bf16_f32 v42, v48, v49
	v_cvt_pk_bf16_f32 v43, v50, v51
	v_cvt_pk_bf16_f32 v44, v52, v53
	v_cvt_pk_bf16_f32 v45, v64, v65
	v_cvt_pk_bf16_f32 v32, v232, v233
	v_cvt_pk_bf16_f32 v33, v234, v235
	v_mfma_f32_32x32x16_bf16 v[0:15], v[38:41], v[42:45], v[0:15]
	v_cvt_pk_bf16_f32 v34, v236, v237
	v_cvt_pk_bf16_f32 v35, v238, v239
	v_cvt_pk_bf16_f32 v38, v58, v59
	v_add_f32_e32 v42, 1.0, v205
	v_div_scale_f32 v43, s[4:5], v42, v42, 1.0
	v_rcp_f32_e32 v44, v43
	v_cvt_pk_bf16_f32 v39, v54, v55
	v_cvt_pk_bf16_f32 v40, v62, v63
	v_cvt_pk_bf16_f32 v41, v60, v61
	s_lshl_b32 s4, s28, 8
	s_or_b32 s4, s4, s12
	v_mfma_f32_32x32x16_bf16 v[0:15], v[32:35], v[38:41], v[0:15]
	v_fma_f32 v32, -v43, v44, 1.0
	v_fmac_f32_e32 v44, v32, v44
	v_div_scale_f32 v32, vcc, 1.0, v42, 1.0
	s_add_i32 s0, s4, s0
	v_mul_f32_e32 v33, v32, v44
	s_lshl_b64 s[0:1], s[0:1], 14
	v_fma_f32 v34, -v43, v33, v32
	s_add_u32 s0, s10, s0
	v_fmac_f32_e32 v33, v34, v44
	s_addc_u32 s1, s11, s1
	v_fma_f32 v32, -v43, v33, v32
	s_add_u32 s0, s0, s2
	v_div_fmas_f32 v32, v32, v44, v33
	s_addc_u32 s1, s1, s3
	v_add_f32_e32 v0, v0, v240
	v_div_fixup_f32 v34, v32, v42, 1.0
	v_lshl_add_u64 v[32:33], s[0:1], 0, v[36:37]
	s_waitcnt vmcnt(0)
	v_fmac_f32_e32 v124, v205, v0
	v_mul_f32_e32 v0, v34, v124
	v_lshl_add_u64 v[32:33], v[32:33], 0, v[122:123]
	global_store_dword v[32:33], v0, off sc1
	v_add_f32_e32 v0, v1, v241
	s_movk_i32 s0, 0x4000
	v_fmac_f32_e32 v125, v205, v0
	v_add_co_u32_e32 v0, vcc, s0, v32
	v_mul_f32_e32 v28, v34, v125
	s_nop 0
	v_addc_co_u32_e32 v1, vcc, 0, v33, vcc
	global_store_dword v[0:1], v28, off sc1
	v_add_f32_e32 v0, v2, v242
	s_mov_b32 s0, 0x8000
	v_fmac_f32_e32 v126, v205, v0
	v_add_co_u32_e32 v0, vcc, s0, v32
	v_mul_f32_e32 v2, v34, v126
	s_nop 0
	v_addc_co_u32_e32 v1, vcc, 0, v33, vcc
	global_store_dword v[0:1], v2, off sc1
	v_add_f32_e32 v0, v3, v243
	s_mov_b32 s0, 0xc000
	v_fmac_f32_e32 v127, v205, v0
	v_add_co_u32_e32 v0, vcc, s0, v32
	v_mul_f32_e32 v2, v34, v127
	s_nop 0
	v_addc_co_u32_e32 v1, vcc, 0, v33, vcc
	global_store_dword v[0:1], v2, off sc1
	v_add_f32_e32 v0, v4, v244
	s_mov_b32 s0, 0x20000
	v_fmac_f32_e32 v128, v205, v0
	v_add_co_u32_e32 v0, vcc, s0, v32
	v_mul_f32_e32 v2, v34, v128
	s_nop 0
	v_addc_co_u32_e32 v1, vcc, 0, v33, vcc
	global_store_dword v[0:1], v2, off sc1
	v_add_f32_e32 v0, v5, v245
	s_mov_b32 s0, 0x24000
	v_fmac_f32_e32 v129, v205, v0
	v_add_co_u32_e32 v0, vcc, s0, v32
	v_mul_f32_e32 v2, v34, v129
	s_nop 0
	v_addc_co_u32_e32 v1, vcc, 0, v33, vcc
	global_store_dword v[0:1], v2, off sc1
	v_add_f32_e32 v0, v6, v246
	s_mov_b32 s0, 0x28000
	v_fmac_f32_e32 v130, v205, v0
	v_add_co_u32_e32 v0, vcc, s0, v32
	v_mul_f32_e32 v2, v34, v130
	s_nop 0
	v_addc_co_u32_e32 v1, vcc, 0, v33, vcc
	global_store_dword v[0:1], v2, off sc1
	v_add_f32_e32 v0, v7, v247
	s_mov_b32 s0, 0x2c000
	v_fmac_f32_e32 v131, v205, v0
	v_add_co_u32_e32 v0, vcc, s0, v32
	v_mul_f32_e32 v2, v34, v131
	s_nop 0
	v_addc_co_u32_e32 v1, vcc, 0, v33, vcc
	global_store_dword v[0:1], v2, off sc1
	v_add_f32_e32 v0, v8, v248
	s_mov_b32 s0, 0x40000
	v_fmac_f32_e32 v132, v205, v0
	v_add_co_u32_e32 v0, vcc, s0, v32
	v_mul_f32_e32 v2, v34, v132
	s_nop 0
	v_addc_co_u32_e32 v1, vcc, 0, v33, vcc
	global_store_dword v[0:1], v2, off sc1
	v_add_f32_e32 v0, v9, v249
	s_mov_b32 s0, 0x44000
	v_fmac_f32_e32 v133, v205, v0
	v_add_co_u32_e32 v0, vcc, s0, v32
	v_mul_f32_e32 v2, v34, v133
	s_nop 0
	v_addc_co_u32_e32 v1, vcc, 0, v33, vcc
	global_store_dword v[0:1], v2, off sc1
	v_add_f32_e32 v0, v10, v250
	s_mov_b32 s0, 0x48000
	v_fmac_f32_e32 v134, v205, v0
	v_add_co_u32_e32 v0, vcc, s0, v32
	v_mul_f32_e32 v2, v34, v134
	s_nop 0
	v_addc_co_u32_e32 v1, vcc, 0, v33, vcc
	global_store_dword v[0:1], v2, off sc1
	v_add_f32_e32 v0, v11, v251
	s_mov_b32 s0, 0x4c000
	v_fmac_f32_e32 v135, v205, v0
	v_add_co_u32_e32 v0, vcc, s0, v32
	v_mul_f32_e32 v2, v34, v135
	s_nop 0
	v_addc_co_u32_e32 v1, vcc, 0, v33, vcc
	global_store_dword v[0:1], v2, off sc1
	v_add_f32_e32 v0, v12, v252
	s_mov_b32 s0, 0x60000
	v_fmac_f32_e32 v136, v205, v0
	v_add_co_u32_e32 v0, vcc, s0, v32
	v_mul_f32_e32 v2, v34, v136
	s_nop 0
	v_addc_co_u32_e32 v1, vcc, 0, v33, vcc
	global_store_dword v[0:1], v2, off sc1
	v_add_f32_e32 v0, v13, v253
	s_mov_b32 s0, 0x64000
	v_fmac_f32_e32 v137, v205, v0
	v_add_co_u32_e32 v0, vcc, s0, v32
	v_mul_f32_e32 v2, v34, v137
	s_nop 0
	v_addc_co_u32_e32 v1, vcc, 0, v33, vcc
	global_store_dword v[0:1], v2, off sc1
	v_add_f32_e32 v0, v14, v254
	s_mov_b32 s0, 0x68000
	v_fmac_f32_e32 v138, v205, v0
	v_add_co_u32_e32 v0, vcc, s0, v32
	v_mul_f32_e32 v2, v34, v138
	s_nop 0
	v_addc_co_u32_e32 v1, vcc, 0, v33, vcc
	global_store_dword v[0:1], v2, off sc1
	v_add_f32_e32 v0, v15, v255
	v_fmac_f32_e32 v139, v205, v0
	v_add_co_u32_e32 v0, vcc, 0x6c000, v32
	v_mul_f32_e32 v2, v34, v139
	s_nop 0
	v_addc_co_u32_e32 v1, vcc, 0, v33, vcc
	global_store_dword v[0:1], v2, off sc1
	s_endpgm
